# baseline (speedup 1.0000x reference)
_Z11edge_kernelILi36ELb1EEvPKfS1_PKDF16_PKiS5_S1_S1_S1_S1_S1_PDF16_:
	s_load_dwordx8 s[4:11], s[0:1], 0x0
	s_load_dwordx8 s[12:19], s[0:1], 0x20
	s_load_dwordx4 s[20:23], s[0:1], 0x40
	s_load_dwordx2 s[24:25], s[0:1], 0x50
	v_readfirstlane_b32 s3, v0
	v_bfe_u32 v75, v0, 4, 2
	v_and_b32_e32 v76, 15, v0
	v_and_b32_e32 v78, 63, v0
	s_lshr_b32 s3, s3, 6
	s_lshl_b32 s2, s2, 1
	s_add_i32 s2, s2, s3
	v_lshlrev_b32_e32 v74, 8, v75
	v_lshl_or_b32 v74, v76, 4, v74
	v_lshlrev_b32_e32 v79, 4, v78
	v_lshl_or_b32 v77, v76, 2, v75
	v_lshlrev_b32_e32 v77, 2, v77
	v_mul_u32_u24_e32 v73, 0x900, v75
	v_lshl_or_b32 v73, v76, 4, v73
	v_mul_u32_u24_e32 v78, 36, v75
	s_mul_i32 s28, s2, 0x2400
	s_lshl_b32 s29, s2, 14
	s_lshl_b32 s30, s2, 2
	s_lshl_b32 s31, s2, 8
	s_lshl_b32 s33, s3, 10
	s_lshl_b32 s34, s3, 8
	s_addk_i32 s34, 0x4000
	s_waitcnt lgkmcnt(0)
	s_add_u32 s10, s10, s30
	s_addc_u32 s11, s11, 0
	s_add_u32 s12, s12, s30
	s_addc_u32 s13, s13, 0
	s_load_dword s35, s[10:11], 0x0
	s_load_dword s36, s[12:13], 0x0
	s_add_u32 s14, s14, s28
	s_addc_u32 s15, s15, 0
	global_load_dwordx4 v[0:3], v73, s[14:15] nt
	global_load_dwordx4 v[4:7], v73, s[14:15] offset:256 nt
	global_load_dwordx4 v[8:11], v73, s[14:15] offset:512 nt
	global_load_dwordx4 v[12:15], v73, s[14:15] offset:768 nt
	global_load_dwordx4 v[16:19], v73, s[14:15] offset:1024 nt
	global_load_dwordx4 v[20:23], v73, s[14:15] offset:1280 nt
	global_load_dwordx4 v[24:27], v73, s[14:15] offset:1536 nt
	global_load_dwordx4 v[28:31], v73, s[14:15] offset:1792 nt
	global_load_dwordx4 v[32:35], v73, s[14:15] offset:2048 nt
	s_add_u32 s22, s22, s33
	s_addc_u32 s23, s23, 0
	s_mov_b32 m0, s33
	s_add_u32 s18, s18, s29
	s_addc_u32 s19, s19, 0
	global_load_lds_dwordx4 v79, s[22:23]
	global_load_lds_dwordx4 v79, s[22:23] offset:2048
	s_add_u32 m0, m0, 0x1000
	s_add_u32 s22, s22, 0x1000
	s_addc_u32 s23, s23, 0
	global_load_lds_dwordx4 v79, s[22:23]
	global_load_lds_dwordx4 v79, s[22:23] offset:2048
	s_add_u32 m0, m0, 0x1000
	s_add_u32 s22, s22, 0x1000
	s_addc_u32 s23, s23, 0
	global_load_lds_dwordx4 v79, s[22:23]
	global_load_lds_dwordx4 v79, s[22:23] offset:2048
	s_add_u32 m0, m0, 0x1000
	s_add_u32 s22, s22, 0x1000
	s_addc_u32 s23, s23, 0
	global_load_lds_dwordx4 v79, s[22:23]
	global_load_lds_dwordx4 v79, s[22:23] offset:2048
	s_add_u32 s16, s16, s31
	s_addc_u32 s17, s17, 0
	s_add_u32 s20, s20, s31
	s_addc_u32 s21, s21, 0
	s_waitcnt lgkmcnt(0)
	s_lshl_b32 s36, s36, 7
	s_add_u32 s24, s24, s36
	s_addc_u32 s25, s25, 0
	s_lshl_b32 s37, s35, 7
	s_lshl_b32 s38, s35, 4
	s_add_u32 s4, s4, s37
	s_addc_u32 s5, s5, 0
	s_add_u32 s6, s6, s38
	s_addc_u32 s7, s7, 0
	v_mov_b32_e32 v93, 0
	v_mov_b32_e32 v92, v78
	v_lshl_add_u64 v[94:95], s[4:5], 0, v[92:93]
	v_lshl_add_u64 v[94:95], v[94:95], 0, 20
	v_cmp_eq_u32_e32 vcc, 3, v75
	s_nop 1
	v_mov_b32_e32 v90, s6
	v_mov_b32_e32 v91, s7
	v_cndmask_b32_e32 v94, v94, v90, vcc
	v_cndmask_b32_e32 v95, v95, v91, vcc
	global_load_dwordx4 v[80:83], v78, s[4:5] nt
	global_load_dword v84, v78, s[4:5] offset:16 nt
	global_load_dwordx4 v[86:89], v[94:95], off nt
	global_load_dword v72, v77, s[16:17] nt
	global_load_dword v64, v77, s[20:21] nt
	v_add_u32_e32 v78, s34, v77
	v_lshl_add_u32 v79, v75, 2, s34
	s_waitcnt vmcnt(2)
	s_barrier
	v_pk_mul_f32 v[96:97], v[80:81], v[0:1] op_sel_hi:[0,1]
	v_pk_mul_f32 v[98:99], v[80:81], v[2:3] op_sel_hi:[0,1]
	v_pk_mul_f32 v[100:101], v[80:81], v[4:5] op_sel:[1,0]
	v_pk_mul_f32 v[102:103], v[80:81], v[6:7] op_sel:[1,0]
	v_pk_fma_f32 v[96:97], v[82:83], v[8:9], v[96:97] op_sel_hi:[0,1,1]
	v_pk_fma_f32 v[98:99], v[82:83], v[10:11], v[98:99] op_sel_hi:[0,1,1]
	v_pk_fma_f32 v[100:101], v[82:83], v[12:13], v[100:101] op_sel:[1,0,0]
	v_pk_fma_f32 v[102:103], v[82:83], v[14:15], v[102:103] op_sel:[1,0,0]
	v_pk_fma_f32 v[96:97], v[84:85], v[16:17], v[96:97] op_sel_hi:[0,1,1]
	v_pk_fma_f32 v[98:99], v[84:85], v[18:19], v[98:99] op_sel_hi:[0,1,1]
	v_pk_fma_f32 v[100:101], v[86:87], v[20:21], v[100:101] op_sel_hi:[0,1,1]
	v_pk_fma_f32 v[102:103], v[86:87], v[22:23], v[102:103] op_sel_hi:[0,1,1]
	v_pk_fma_f32 v[96:97], v[86:87], v[24:25], v[96:97] op_sel:[1,0,0]
	v_pk_fma_f32 v[98:99], v[86:87], v[26:27], v[98:99] op_sel:[1,0,0]
	v_pk_fma_f32 v[100:101], v[88:89], v[28:29], v[100:101] op_sel_hi:[0,1,1]
	v_pk_fma_f32 v[102:103], v[88:89], v[30:31], v[102:103] op_sel_hi:[0,1,1]
	v_pk_fma_f32 v[96:97], v[88:89], v[32:33], v[96:97] op_sel:[1,0,0]
	v_pk_fma_f32 v[98:99], v[88:89], v[34:35], v[98:99] op_sel:[1,0,0]
	v_pk_add_f32 v[96:97], v[96:97], v[100:101]
	v_pk_add_f32 v[98:99], v[98:99], v[102:103]
	s_nop 1
	v_permlane16_swap_b32_e32 v96, v97
	v_permlane16_swap_b32_e32 v98, v99
	v_add_f32_e32 v96, v96, v97
	v_add_f32_e32 v98, v98, v99
	s_nop 1
	v_permlane32_swap_b32_e32 v96, v98
	v_add_f32_e32 v96, v96, v98
	s_waitcnt vmcnt(1)
	v_add_f32_e32 v96, v96, v72
	v_max_f32_e32 v96, 0, v96
	ds_write_b32 v78, v96
	ds_read2_b32 v[80:81], v79 offset0:0 offset1:4
	ds_read2_b32 v[82:83], v79 offset0:8 offset1:12
	ds_read2_b32 v[84:85], v79 offset0:16 offset1:20
	ds_read2_b32 v[86:87], v79 offset0:24 offset1:28
	ds_read2_b32 v[88:89], v79 offset0:32 offset1:36
	ds_read2_b32 v[90:91], v79 offset0:40 offset1:44
	ds_read2_b32 v[92:93], v79 offset0:48 offset1:52
	ds_read2_b32 v[94:95], v79 offset0:56 offset1:60
	s_waitcnt lgkmcnt(0)
	v_cmp_neq_f32_e64 s[40:41], 0, v80
	v_cmp_neq_f32_e64 s[42:43], 0, v81
	v_cmp_neq_f32_e64 s[44:45], 0, v82
	v_cmp_neq_f32_e64 s[46:47], 0, v83
	v_cmp_neq_f32_e64 s[48:49], 0, v84
	v_cmp_neq_f32_e64 s[50:51], 0, v85
	v_cmp_neq_f32_e64 s[52:53], 0, v86
	v_cmp_neq_f32_e64 s[54:55], 0, v87
	v_cmp_neq_f32_e64 s[56:57], 0, v88
	v_cmp_neq_f32_e64 s[58:59], 0, v89
	v_cmp_neq_f32_e64 s[60:61], 0, v90
	v_cmp_neq_f32_e64 s[62:63], 0, v91
	v_cmp_neq_f32_e64 s[64:65], 0, v92
	v_cmp_neq_f32_e64 s[66:67], 0, v93
	v_cmp_neq_f32_e64 s[68:69], 0, v94
	v_cmp_neq_f32_e64 s[70:71], 0, v95
	s_mov_b64 exec, s[40:41]
	global_load_dwordx4 v[0:3], v74, s[18:19] nt
	s_mov_b64 exec, s[42:43]
	global_load_dwordx4 v[4:7], v74, s[18:19] offset:1024 nt
	s_mov_b64 exec, s[44:45]
	global_load_dwordx4 v[8:11], v74, s[18:19] offset:2048 nt
	s_mov_b64 exec, s[46:47]
	global_load_dwordx4 v[12:15], v74, s[18:19] offset:3072 nt
	s_add_u32 s18, s18, 0x1000
	s_addc_u32 s19, s19, 0
	s_mov_b64 exec, s[48:49]
	global_load_dwordx4 v[16:19], v74, s[18:19] nt
	s_mov_b64 exec, s[50:51]
	global_load_dwordx4 v[20:23], v74, s[18:19] offset:1024 nt
	s_mov_b64 exec, s[52:53]
	global_load_dwordx4 v[24:27], v74, s[18:19] offset:2048 nt
	s_mov_b64 exec, s[54:55]
	global_load_dwordx4 v[28:31], v74, s[18:19] offset:3072 nt
	s_add_u32 s18, s18, 0x1000
	s_addc_u32 s19, s19, 0
	s_mov_b64 exec, s[56:57]
	global_load_dwordx4 v[32:35], v74, s[18:19] nt
	s_mov_b64 exec, s[58:59]
	global_load_dwordx4 v[36:39], v74, s[18:19] offset:1024 nt
	s_mov_b64 exec, s[60:61]
	global_load_dwordx4 v[40:43], v74, s[18:19] offset:2048 nt
	s_mov_b64 exec, s[62:63]
	global_load_dwordx4 v[44:47], v74, s[18:19] offset:3072 nt
	s_add_u32 s18, s18, 0x1000
	s_addc_u32 s19, s19, 0
	s_mov_b64 exec, s[64:65]
	global_load_dwordx4 v[48:51], v74, s[18:19] nt
	s_mov_b64 exec, s[66:67]
	global_load_dwordx4 v[52:55], v74, s[18:19] offset:1024 nt
	s_mov_b64 exec, s[68:69]
	global_load_dwordx4 v[56:59], v74, s[18:19] offset:2048 nt
	s_mov_b64 exec, s[70:71]
	global_load_dwordx4 v[60:63], v74, s[18:19] offset:3072 nt
	s_mov_b64 exec, -1
	v_mov_b32_e32 v96, 0
	v_mov_b32_e32 v97, 0
	v_mov_b32_e32 v98, 0
	v_mov_b32_e32 v99, 0
	v_mov_b32_e32 v100, 0
	v_mov_b32_e32 v101, 0
	v_mov_b32_e32 v102, 0
	v_mov_b32_e32 v103, 0
	s_waitcnt vmcnt(0)
	s_mov_b64 exec, s[40:41]
	v_pk_fma_f32 v[96:97], v[80:81], v[0:1], v[96:97] op_sel_hi:[0,1,1]
	v_pk_fma_f32 v[98:99], v[80:81], v[2:3], v[98:99] op_sel_hi:[0,1,1]
	s_mov_b64 exec, s[42:43]
	v_pk_fma_f32 v[100:101], v[80:81], v[4:5], v[100:101] op_sel:[1,0,0]
	v_pk_fma_f32 v[102:103], v[80:81], v[6:7], v[102:103] op_sel:[1,0,0]
	s_mov_b64 exec, s[44:45]
	v_pk_fma_f32 v[96:97], v[82:83], v[8:9], v[96:97] op_sel_hi:[0,1,1]
	v_pk_fma_f32 v[98:99], v[82:83], v[10:11], v[98:99] op_sel_hi:[0,1,1]
	s_mov_b64 exec, s[46:47]
	v_pk_fma_f32 v[100:101], v[82:83], v[12:13], v[100:101] op_sel:[1,0,0]
	v_pk_fma_f32 v[102:103], v[82:83], v[14:15], v[102:103] op_sel:[1,0,0]
	s_mov_b64 exec, s[48:49]
	v_pk_fma_f32 v[96:97], v[84:85], v[16:17], v[96:97] op_sel_hi:[0,1,1]
	v_pk_fma_f32 v[98:99], v[84:85], v[18:19], v[98:99] op_sel_hi:[0,1,1]
	s_mov_b64 exec, s[50:51]
	v_pk_fma_f32 v[100:101], v[84:85], v[20:21], v[100:101] op_sel:[1,0,0]
	v_pk_fma_f32 v[102:103], v[84:85], v[22:23], v[102:103] op_sel:[1,0,0]
	s_mov_b64 exec, s[52:53]
	v_pk_fma_f32 v[96:97], v[86:87], v[24:25], v[96:97] op_sel_hi:[0,1,1]
	v_pk_fma_f32 v[98:99], v[86:87], v[26:27], v[98:99] op_sel_hi:[0,1,1]
	s_mov_b64 exec, s[54:55]
	v_pk_fma_f32 v[100:101], v[86:87], v[28:29], v[100:101] op_sel:[1,0,0]
	v_pk_fma_f32 v[102:103], v[86:87], v[30:31], v[102:103] op_sel:[1,0,0]
	s_mov_b64 exec, s[56:57]
	v_pk_fma_f32 v[96:97], v[88:89], v[32:33], v[96:97] op_sel_hi:[0,1,1]
	v_pk_fma_f32 v[98:99], v[88:89], v[34:35], v[98:99] op_sel_hi:[0,1,1]
	s_mov_b64 exec, s[58:59]
	v_pk_fma_f32 v[100:101], v[88:89], v[36:37], v[100:101] op_sel:[1,0,0]
	v_pk_fma_f32 v[102:103], v[88:89], v[38:39], v[102:103] op_sel:[1,0,0]
	s_mov_b64 exec, s[60:61]
	v_pk_fma_f32 v[96:97], v[90:91], v[40:41], v[96:97] op_sel_hi:[0,1,1]
	v_pk_fma_f32 v[98:99], v[90:91], v[42:43], v[98:99] op_sel_hi:[0,1,1]
	s_mov_b64 exec, s[62:63]
	v_pk_fma_f32 v[100:101], v[90:91], v[44:45], v[100:101] op_sel:[1,0,0]
	v_pk_fma_f32 v[102:103], v[90:91], v[46:47], v[102:103] op_sel:[1,0,0]
	s_mov_b64 exec, s[64:65]
	v_pk_fma_f32 v[96:97], v[92:93], v[48:49], v[96:97] op_sel_hi:[0,1,1]
	v_pk_fma_f32 v[98:99], v[92:93], v[50:51], v[98:99] op_sel_hi:[0,1,1]
	s_mov_b64 exec, s[66:67]
	v_pk_fma_f32 v[100:101], v[92:93], v[52:53], v[100:101] op_sel:[1,0,0]
	v_pk_fma_f32 v[102:103], v[92:93], v[54:55], v[102:103] op_sel:[1,0,0]
	s_mov_b64 exec, s[68:69]
	v_pk_fma_f32 v[96:97], v[94:95], v[56:57], v[96:97] op_sel_hi:[0,1,1]
	v_pk_fma_f32 v[98:99], v[94:95], v[58:59], v[98:99] op_sel_hi:[0,1,1]
	s_mov_b64 exec, s[70:71]
	v_pk_fma_f32 v[100:101], v[94:95], v[60:61], v[100:101] op_sel:[1,0,0]
	v_pk_fma_f32 v[102:103], v[94:95], v[62:63], v[102:103] op_sel:[1,0,0]
	s_mov_b64 exec, -1
	ds_read_b128 v[0:3], v74
	ds_read_b128 v[4:7], v74 offset:1024
	ds_read_b128 v[8:11], v74 offset:2048
	ds_read_b128 v[12:15], v74 offset:3072
	ds_read_b128 v[16:19], v74 offset:4096
	ds_read_b128 v[20:23], v74 offset:5120
	ds_read_b128 v[24:27], v74 offset:6144
	ds_read_b128 v[28:31], v74 offset:7168
	ds_read_b128 v[32:35], v74 offset:8192
	ds_read_b128 v[36:39], v74 offset:9216
	ds_read_b128 v[40:43], v74 offset:10240
	ds_read_b128 v[44:47], v74 offset:11264
	ds_read_b128 v[48:51], v74 offset:12288
	ds_read_b128 v[52:55], v74 offset:13312
	ds_read_b128 v[56:59], v74 offset:14336
	v_pk_add_f32 v[96:97], v[96:97], v[100:101]
	v_pk_add_f32 v[98:99], v[98:99], v[102:103]
	s_nop 1
	v_permlane16_swap_b32_e32 v96, v97
	v_permlane16_swap_b32_e32 v98, v99
	v_add_f32_e32 v96, v96, v97
	v_add_f32_e32 v98, v98, v99
	s_nop 1
	v_permlane32_swap_b32_e32 v96, v98
	v_add_f32_e32 v96, v96, v98
	v_add_f32_e32 v96, v96, v64
	s_waitcnt lgkmcnt(5)
	ds_read_b128 v[60:63], v74 offset:15360
	ds_write_b32 v78, v96
	ds_read2_b32 v[80:81], v79 offset0:0 offset1:4
	ds_read2_b32 v[82:83], v79 offset0:8 offset1:12
	ds_read2_b32 v[84:85], v79 offset0:16 offset1:20
	ds_read2_b32 v[86:87], v79 offset0:24 offset1:28
	ds_read2_b32 v[88:89], v79 offset0:32 offset1:36
	ds_read2_b32 v[90:91], v79 offset0:40 offset1:44
	ds_read2_b32 v[92:93], v79 offset0:48 offset1:52
	ds_read2_b32 v[94:95], v79 offset0:56 offset1:60
	v_lshlrev_b32_e32 v72, 3, v76
	v_lshl_or_b32 v72, v75, 2, v72
	v_cmp_gt_u32_e32 vcc, 2, v75
	s_waitcnt lgkmcnt(0)
	v_pk_mul_f32 v[96:97], v[80:81], v[0:1] op_sel_hi:[0,1]
	v_pk_mul_f32 v[98:99], v[80:81], v[2:3] op_sel_hi:[0,1]
	v_pk_mul_f32 v[100:101], v[80:81], v[4:5] op_sel:[1,0]
	v_pk_mul_f32 v[102:103], v[80:81], v[6:7] op_sel:[1,0]
	v_pk_fma_f32 v[96:97], v[82:83], v[8:9], v[96:97] op_sel_hi:[0,1,1]
	v_pk_fma_f32 v[98:99], v[82:83], v[10:11], v[98:99] op_sel_hi:[0,1,1]
	v_pk_fma_f32 v[100:101], v[82:83], v[12:13], v[100:101] op_sel:[1,0,0]
	v_pk_fma_f32 v[102:103], v[82:83], v[14:15], v[102:103] op_sel:[1,0,0]
	v_pk_fma_f32 v[96:97], v[84:85], v[16:17], v[96:97] op_sel_hi:[0,1,1]
	v_pk_fma_f32 v[98:99], v[84:85], v[18:19], v[98:99] op_sel_hi:[0,1,1]
	v_pk_fma_f32 v[100:101], v[84:85], v[20:21], v[100:101] op_sel:[1,0,0]
	v_pk_fma_f32 v[102:103], v[84:85], v[22:23], v[102:103] op_sel:[1,0,0]
	v_pk_fma_f32 v[96:97], v[86:87], v[24:25], v[96:97] op_sel_hi:[0,1,1]
	v_pk_fma_f32 v[98:99], v[86:87], v[26:27], v[98:99] op_sel_hi:[0,1,1]
	v_pk_fma_f32 v[100:101], v[86:87], v[28:29], v[100:101] op_sel:[1,0,0]
	v_pk_fma_f32 v[102:103], v[86:87], v[30:31], v[102:103] op_sel:[1,0,0]
	v_pk_fma_f32 v[96:97], v[88:89], v[32:33], v[96:97] op_sel_hi:[0,1,1]
	v_pk_fma_f32 v[98:99], v[88:89], v[34:35], v[98:99] op_sel_hi:[0,1,1]
	v_pk_fma_f32 v[100:101], v[88:89], v[36:37], v[100:101] op_sel:[1,0,0]
	v_pk_fma_f32 v[102:103], v[88:89], v[38:39], v[102:103] op_sel:[1,0,0]
	v_pk_fma_f32 v[96:97], v[90:91], v[40:41], v[96:97] op_sel_hi:[0,1,1]
	v_pk_fma_f32 v[98:99], v[90:91], v[42:43], v[98:99] op_sel_hi:[0,1,1]
	v_pk_fma_f32 v[100:101], v[90:91], v[44:45], v[100:101] op_sel:[1,0,0]
	v_pk_fma_f32 v[102:103], v[90:91], v[46:47], v[102:103] op_sel:[1,0,0]
	v_pk_fma_f32 v[96:97], v[92:93], v[48:49], v[96:97] op_sel_hi:[0,1,1]
	v_pk_fma_f32 v[98:99], v[92:93], v[50:51], v[98:99] op_sel_hi:[0,1,1]
	v_pk_fma_f32 v[100:101], v[92:93], v[52:53], v[100:101] op_sel:[1,0,0]
	v_pk_fma_f32 v[102:103], v[92:93], v[54:55], v[102:103] op_sel:[1,0,0]
	v_pk_fma_f32 v[96:97], v[94:95], v[56:57], v[96:97] op_sel_hi:[0,1,1]
	v_pk_fma_f32 v[98:99], v[94:95], v[58:59], v[98:99] op_sel_hi:[0,1,1]
	v_pk_fma_f32 v[100:101], v[94:95], v[60:61], v[100:101] op_sel:[1,0,0]
	v_pk_fma_f32 v[102:103], v[94:95], v[62:63], v[102:103] op_sel:[1,0,0]
	v_pk_add_f32 v[96:97], v[96:97], v[100:101]
	v_pk_add_f32 v[98:99], v[98:99], v[102:103]
	s_nop 1
	v_permlane16_swap_b32_e32 v96, v98
	v_permlane16_swap_b32_e32 v97, v99
	v_add_f32_e32 v96, v96, v98
	v_add_f32_e32 v97, v97, v99
	v_mov_b32_e32 v80, v96
	v_mov_b32_e32 v81, v97
	s_nop 1
	v_permlane32_swap_b32_e32 v96, v80
	v_permlane32_swap_b32_e32 v97, v81
	v_add_f32_e32 v96, v96, v80
	v_add_f32_e32 v97, v97, v81
	v_cvt_pk_f16_f32 v73, v96, v97
	s_and_saveexec_b64 s[4:5], vcc
	global_atomic_pk_add_f16 v72, v73, s[24:25]
	s_endpgm
	.p2align	8

	.amdhsa_kernel _Z11edge_kernelILi36ELb1EEvPKfS1_PKDF16_PKiS5_S1_S1_S1_S1_S1_PDF16_
		.amdhsa_group_segment_fixed_size 16896
		.amdhsa_private_segment_fixed_size 0
		.amdhsa_kernarg_size 88
		.amdhsa_user_sgpr_count 2
		.amdhsa_user_sgpr_dispatch_ptr 0
		.amdhsa_user_sgpr_queue_ptr 0
		.amdhsa_user_sgpr_kernarg_segment_ptr 1
		.amdhsa_user_sgpr_dispatch_id 0
		.amdhsa_user_sgpr_kernarg_preload_length 0
		.amdhsa_user_sgpr_kernarg_preload_offset 0
		.amdhsa_user_sgpr_private_segment_size 0
		.amdhsa_uses_dynamic_stack 0
		.amdhsa_enable_private_segment 0
		.amdhsa_system_sgpr_workgroup_id_x 1
		.amdhsa_system_sgpr_workgroup_id_y 0
		.amdhsa_system_sgpr_workgroup_id_z 0
		.amdhsa_system_sgpr_workgroup_info 0
		.amdhsa_system_vgpr_workitem_id 0
		.amdhsa_next_free_vgpr 104
		.amdhsa_next_free_sgpr 96
		.amdhsa_accum_offset 104
		.amdhsa_reserve_vcc 1
		.amdhsa_float_round_mode_32 0
		.amdhsa_float_round_mode_16_64 0
		.amdhsa_float_denorm_mode_32 3
		.amdhsa_float_denorm_mode_16_64 3
		.amdhsa_dx10_clamp 1
		.amdhsa_ieee_mode 1
		.amdhsa_fp16_overflow 0
		.amdhsa_tg_split 0
		.amdhsa_exception_fp_ieee_invalid_op 0
		.amdhsa_exception_fp_denorm_src 0
		.amdhsa_exception_fp_ieee_div_zero 0
		.amdhsa_exception_fp_ieee_overflow 0
		.amdhsa_exception_fp_ieee_underflow 0
		.amdhsa_exception_fp_ieee_inexact 0
		.amdhsa_exception_int_div_zero 0
	.end_amdhsa_kernel

_Z11edge_kernelILi64ELb0EEvPKfS1_PKDF16_PKiS5_S1_S1_S1_S1_S1_PDF16_:
	s_load_dwordx16 s[4:19], s[0:1], 0x10
	s_load_dwordx2 s[20:21], s[0:1], 0x50
	v_readfirstlane_b32 s3, v0
	v_bfe_u32 v75, v0, 4, 2
	v_and_b32_e32 v76, 15, v0
	v_and_b32_e32 v78, 63, v0
	s_lshr_b32 s3, s3, 6
	s_lshl_b32 s2, s2, 1
	s_add_i32 s2, s2, s3
	v_lshlrev_b32_e32 v74, 8, v75
	v_lshl_or_b32 v74, v76, 4, v74
	v_lshlrev_b32_e32 v79, 4, v78
	v_lshl_or_b32 v77, v76, 2, v75
	v_lshlrev_b32_e32 v77, 2, v77
	v_lshlrev_b32_e32 v78, 5, v75
	v_lshlrev_b32_e32 v73, 12, v75
	v_lshl_or_b32 v73, v76, 4, v73
	s_lshl_b32 s28, s2, 14
	s_lshl_b32 s29, s2, 14
	s_lshl_b32 s30, s2, 2
	s_lshl_b32 s31, s2, 8
	s_lshl_b32 s33, s3, 10
	s_lshl_b32 s34, s3, 8
	s_addk_i32 s34, 0x4000
	s_waitcnt lgkmcnt(0)
	s_add_u32 s6, s6, s30
	s_addc_u32 s7, s7, 0
	s_add_u32 s8, s8, s30
	s_addc_u32 s9, s9, 0
	s_load_dword s35, s[6:7], 0x0
	s_load_dword s36, s[8:9], 0x0
	s_add_u32 s10, s10, s28
	s_addc_u32 s11, s11, 0
	s_add_u32 s18, s18, s33
	s_addc_u32 s19, s19, 0
	s_mov_b32 m0, s33
	s_add_u32 s14, s14, s29
	s_addc_u32 s15, s15, 0
	global_load_lds_dwordx4 v79, s[18:19]
	global_load_lds_dwordx4 v79, s[18:19] offset:2048
	s_add_u32 m0, m0, 0x1000
	s_add_u32 s18, s18, 0x1000
	s_addc_u32 s19, s19, 0
	global_load_lds_dwordx4 v79, s[18:19]
	global_load_lds_dwordx4 v79, s[18:19] offset:2048
	s_add_u32 m0, m0, 0x1000
	s_add_u32 s18, s18, 0x1000
	s_addc_u32 s19, s19, 0
	global_load_lds_dwordx4 v79, s[18:19]
	global_load_lds_dwordx4 v79, s[18:19] offset:2048
	s_add_u32 m0, m0, 0x1000
	s_add_u32 s18, s18, 0x1000
	s_addc_u32 s19, s19, 0
	global_load_lds_dwordx4 v79, s[18:19]
	global_load_lds_dwordx4 v79, s[18:19] offset:2048
	s_add_u32 s12, s12, s31
	s_addc_u32 s13, s13, 0
	s_add_u32 s16, s16, s31
	s_addc_u32 s17, s17, 0
	s_waitcnt lgkmcnt(0)
	s_lshl_b32 s36, s36, 7
	s_add_u32 s20, s20, s36
	s_addc_u32 s21, s21, 0
	s_lshl_b32 s37, s35, 7
	s_add_u32 s4, s4, s37
	s_addc_u32 s5, s5, 0
	global_load_dwordx4 v[64:67], v78, s[4:5] nt
	global_load_dwordx4 v[68:71], v78, s[4:5] offset:16 nt
	global_load_dword v72, v77, s[12:13] nt
	global_load_dword v73, v77, s[16:17] nt
	v_add_u32_e32 v78, s34, v77
	v_lshl_add_u32 v79, v75, 2, s34
	s_waitcnt vmcnt(2)
	s_barrier
	v_cvt_f32_f16_e32 v80, v64
	v_cvt_f32_f16_sdwa v81, v64 dst_sel:DWORD dst_unused:UNUSED_PAD src0_sel:WORD_1
	v_cvt_f32_f16_e32 v82, v65
	v_cvt_f32_f16_sdwa v83, v65 dst_sel:DWORD dst_unused:UNUSED_PAD src0_sel:WORD_1
	v_cvt_f32_f16_e32 v84, v66
	v_cvt_f32_f16_sdwa v85, v66 dst_sel:DWORD dst_unused:UNUSED_PAD src0_sel:WORD_1
	v_cvt_f32_f16_e32 v86, v67
	v_cvt_f32_f16_sdwa v87, v67 dst_sel:DWORD dst_unused:UNUSED_PAD src0_sel:WORD_1
	v_cvt_f32_f16_e32 v88, v68
	v_cvt_f32_f16_sdwa v89, v68 dst_sel:DWORD dst_unused:UNUSED_PAD src0_sel:WORD_1
	v_cvt_f32_f16_e32 v90, v69
	v_cvt_f32_f16_sdwa v91, v69 dst_sel:DWORD dst_unused:UNUSED_PAD src0_sel:WORD_1
	v_cvt_f32_f16_e32 v92, v70
	v_cvt_f32_f16_sdwa v93, v70 dst_sel:DWORD dst_unused:UNUSED_PAD src0_sel:WORD_1
	v_cvt_f32_f16_e32 v94, v71
	v_cvt_f32_f16_sdwa v95, v71 dst_sel:DWORD dst_unused:UNUSED_PAD src0_sel:WORD_1
	v_max_f32_e32 v80, 0, v80
	v_max_f32_e32 v81, 0, v81
	v_max_f32_e32 v82, 0, v82
	v_max_f32_e32 v83, 0, v83
	v_max_f32_e32 v84, 0, v84
	v_max_f32_e32 v85, 0, v85
	v_max_f32_e32 v86, 0, v86
	v_max_f32_e32 v87, 0, v87
	v_max_f32_e32 v88, 0, v88
	v_max_f32_e32 v89, 0, v89
	v_max_f32_e32 v90, 0, v90
	v_max_f32_e32 v91, 0, v91
	v_max_f32_e32 v92, 0, v92
	v_max_f32_e32 v93, 0, v93
	v_max_f32_e32 v94, 0, v94
	v_max_f32_e32 v95, 0, v95
	v_cmp_neq_f32_e64 s[40:41], 0, v80
	v_cmp_neq_f32_e64 s[42:43], 0, v81
	v_cmp_neq_f32_e64 s[44:45], 0, v82
	v_cmp_neq_f32_e64 s[46:47], 0, v83
	v_cmp_neq_f32_e64 s[48:49], 0, v84
	v_cmp_neq_f32_e64 s[50:51], 0, v85
	v_cmp_neq_f32_e64 s[52:53], 0, v86
	v_cmp_neq_f32_e64 s[54:55], 0, v87
	v_cmp_neq_f32_e64 s[56:57], 0, v88
	v_cmp_neq_f32_e64 s[58:59], 0, v89
	v_cmp_neq_f32_e64 s[60:61], 0, v90
	v_cmp_neq_f32_e64 s[62:63], 0, v91
	v_cmp_neq_f32_e64 s[64:65], 0, v92
	v_cmp_neq_f32_e64 s[66:67], 0, v93
	v_cmp_neq_f32_e64 s[68:69], 0, v94
	v_cmp_neq_f32_e64 s[70:71], 0, v95
	v_lshlrev_b32_e32 v96, 12, v75
	v_lshl_or_b32 v96, v76, 4, v96
	s_mov_b64 exec, s[40:41]
	global_load_dwordx4 v[0:3], v96, s[10:11] nt
	s_mov_b64 exec, s[42:43]
	global_load_dwordx4 v[4:7], v96, s[10:11] offset:256 nt
	s_mov_b64 exec, s[44:45]
	global_load_dwordx4 v[8:11], v96, s[10:11] offset:512 nt
	s_mov_b64 exec, s[46:47]
	global_load_dwordx4 v[12:15], v96, s[10:11] offset:768 nt
	s_mov_b64 exec, s[48:49]
	global_load_dwordx4 v[16:19], v96, s[10:11] offset:1024 nt
	s_mov_b64 exec, s[50:51]
	global_load_dwordx4 v[20:23], v96, s[10:11] offset:1280 nt
	s_mov_b64 exec, s[52:53]
	global_load_dwordx4 v[24:27], v96, s[10:11] offset:1536 nt
	s_mov_b64 exec, s[54:55]
	global_load_dwordx4 v[28:31], v96, s[10:11] offset:1792 nt
	s_mov_b64 exec, s[56:57]
	global_load_dwordx4 v[32:35], v96, s[10:11] offset:2048 nt
	s_mov_b64 exec, s[58:59]
	global_load_dwordx4 v[36:39], v96, s[10:11] offset:2304 nt
	s_mov_b64 exec, s[60:61]
	global_load_dwordx4 v[40:43], v96, s[10:11] offset:2560 nt
	s_mov_b64 exec, s[62:63]
	global_load_dwordx4 v[44:47], v96, s[10:11] offset:2816 nt
	s_mov_b64 exec, s[64:65]
	global_load_dwordx4 v[48:51], v96, s[10:11] offset:3072 nt
	s_mov_b64 exec, s[66:67]
	global_load_dwordx4 v[52:55], v96, s[10:11] offset:3328 nt
	s_mov_b64 exec, s[68:69]
	global_load_dwordx4 v[56:59], v96, s[10:11] offset:3584 nt
	s_mov_b64 exec, s[70:71]
	global_load_dwordx4 v[60:63], v96, s[10:11] offset:3840 nt
	s_mov_b64 exec, -1
	v_mov_b32_e32 v96, 0
	v_mov_b32_e32 v97, 0
	v_mov_b32_e32 v98, 0
	v_mov_b32_e32 v99, 0
	v_mov_b32_e32 v100, 0
	v_mov_b32_e32 v101, 0
	v_mov_b32_e32 v102, 0
	v_mov_b32_e32 v103, 0
	s_waitcnt vmcnt(0)
	s_mov_b64 exec, s[40:41]
	v_pk_fma_f32 v[96:97], v[80:81], v[0:1], v[96:97] op_sel_hi:[0,1,1]
	v_pk_fma_f32 v[98:99], v[80:81], v[2:3], v[98:99] op_sel_hi:[0,1,1]
	s_mov_b64 exec, s[42:43]
	v_pk_fma_f32 v[100:101], v[80:81], v[4:5], v[100:101] op_sel:[1,0,0]
	v_pk_fma_f32 v[102:103], v[80:81], v[6:7], v[102:103] op_sel:[1,0,0]
	s_mov_b64 exec, s[44:45]
	v_pk_fma_f32 v[96:97], v[82:83], v[8:9], v[96:97] op_sel_hi:[0,1,1]
	v_pk_fma_f32 v[98:99], v[82:83], v[10:11], v[98:99] op_sel_hi:[0,1,1]
	s_mov_b64 exec, s[46:47]
	v_pk_fma_f32 v[100:101], v[82:83], v[12:13], v[100:101] op_sel:[1,0,0]
	v_pk_fma_f32 v[102:103], v[82:83], v[14:15], v[102:103] op_sel:[1,0,0]
	s_mov_b64 exec, s[48:49]
	v_pk_fma_f32 v[96:97], v[84:85], v[16:17], v[96:97] op_sel_hi:[0,1,1]
	v_pk_fma_f32 v[98:99], v[84:85], v[18:19], v[98:99] op_sel_hi:[0,1,1]
	s_mov_b64 exec, s[50:51]
	v_pk_fma_f32 v[100:101], v[84:85], v[20:21], v[100:101] op_sel:[1,0,0]
	v_pk_fma_f32 v[102:103], v[84:85], v[22:23], v[102:103] op_sel:[1,0,0]
	s_mov_b64 exec, s[52:53]
	v_pk_fma_f32 v[96:97], v[86:87], v[24:25], v[96:97] op_sel_hi:[0,1,1]
	v_pk_fma_f32 v[98:99], v[86:87], v[26:27], v[98:99] op_sel_hi:[0,1,1]
	s_mov_b64 exec, s[54:55]
	v_pk_fma_f32 v[100:101], v[86:87], v[28:29], v[100:101] op_sel:[1,0,0]
	v_pk_fma_f32 v[102:103], v[86:87], v[30:31], v[102:103] op_sel:[1,0,0]
	s_mov_b64 exec, s[56:57]
	v_pk_fma_f32 v[96:97], v[88:89], v[32:33], v[96:97] op_sel_hi:[0,1,1]
	v_pk_fma_f32 v[98:99], v[88:89], v[34:35], v[98:99] op_sel_hi:[0,1,1]
	s_mov_b64 exec, s[58:59]
	v_pk_fma_f32 v[100:101], v[88:89], v[36:37], v[100:101] op_sel:[1,0,0]
	v_pk_fma_f32 v[102:103], v[88:89], v[38:39], v[102:103] op_sel:[1,0,0]
	s_mov_b64 exec, s[60:61]
	v_pk_fma_f32 v[96:97], v[90:91], v[40:41], v[96:97] op_sel_hi:[0,1,1]
	v_pk_fma_f32 v[98:99], v[90:91], v[42:43], v[98:99] op_sel_hi:[0,1,1]
	s_mov_b64 exec, s[62:63]
	v_pk_fma_f32 v[100:101], v[90:91], v[44:45], v[100:101] op_sel:[1,0,0]
	v_pk_fma_f32 v[102:103], v[90:91], v[46:47], v[102:103] op_sel:[1,0,0]
	s_mov_b64 exec, s[64:65]
	v_pk_fma_f32 v[96:97], v[92:93], v[48:49], v[96:97] op_sel_hi:[0,1,1]
	v_pk_fma_f32 v[98:99], v[92:93], v[50:51], v[98:99] op_sel_hi:[0,1,1]
	s_mov_b64 exec, s[66:67]
	v_pk_fma_f32 v[100:101], v[92:93], v[52:53], v[100:101] op_sel:[1,0,0]
	v_pk_fma_f32 v[102:103], v[92:93], v[54:55], v[102:103] op_sel:[1,0,0]
	s_mov_b64 exec, s[68:69]
	v_pk_fma_f32 v[96:97], v[94:95], v[56:57], v[96:97] op_sel_hi:[0,1,1]
	v_pk_fma_f32 v[98:99], v[94:95], v[58:59], v[98:99] op_sel_hi:[0,1,1]
	s_mov_b64 exec, s[70:71]
	v_pk_fma_f32 v[100:101], v[94:95], v[60:61], v[100:101] op_sel:[1,0,0]
	v_pk_fma_f32 v[102:103], v[94:95], v[62:63], v[102:103] op_sel:[1,0,0]
	s_mov_b64 exec, -1
	v_pk_add_f32 v[96:97], v[96:97], v[100:101]
	v_pk_add_f32 v[98:99], v[98:99], v[102:103]
	s_nop 1
	v_permlane16_swap_b32_e32 v96, v97
	v_permlane16_swap_b32_e32 v98, v99
	v_add_f32_e32 v96, v96, v97
	v_add_f32_e32 v98, v98, v99
	s_nop 1
	v_permlane32_swap_b32_e32 v96, v98
	v_add_f32_e32 v96, v96, v98
	s_waitcnt vmcnt(17)
	v_add_f32_e32 v96, v96, v72
	v_max_f32_e32 v96, 0, v96
	ds_write_b32 v78, v96
	ds_read2_b32 v[80:81], v79 offset0:0 offset1:4
	ds_read2_b32 v[82:83], v79 offset0:8 offset1:12
	ds_read2_b32 v[84:85], v79 offset0:16 offset1:20
	ds_read2_b32 v[86:87], v79 offset0:24 offset1:28
	ds_read2_b32 v[88:89], v79 offset0:32 offset1:36
	ds_read2_b32 v[90:91], v79 offset0:40 offset1:44
	ds_read2_b32 v[92:93], v79 offset0:48 offset1:52
	ds_read2_b32 v[94:95], v79 offset0:56 offset1:60
	s_waitcnt lgkmcnt(0)
	v_cmp_neq_f32_e64 s[40:41], 0, v80
	v_cmp_neq_f32_e64 s[42:43], 0, v81
	v_cmp_neq_f32_e64 s[44:45], 0, v82
	v_cmp_neq_f32_e64 s[46:47], 0, v83
	v_cmp_neq_f32_e64 s[48:49], 0, v84
	v_cmp_neq_f32_e64 s[50:51], 0, v85
	v_cmp_neq_f32_e64 s[52:53], 0, v86
	v_cmp_neq_f32_e64 s[54:55], 0, v87
	v_cmp_neq_f32_e64 s[56:57], 0, v88
	v_cmp_neq_f32_e64 s[58:59], 0, v89
	v_cmp_neq_f32_e64 s[60:61], 0, v90
	v_cmp_neq_f32_e64 s[62:63], 0, v91
	v_cmp_neq_f32_e64 s[64:65], 0, v92
	v_cmp_neq_f32_e64 s[66:67], 0, v93
	v_cmp_neq_f32_e64 s[68:69], 0, v94
	v_cmp_neq_f32_e64 s[70:71], 0, v95
	s_mov_b64 exec, s[40:41]
	global_load_dwordx4 v[0:3], v74, s[14:15] nt
	s_mov_b64 exec, s[42:43]
	global_load_dwordx4 v[4:7], v74, s[14:15] offset:1024 nt
	s_mov_b64 exec, s[44:45]
	global_load_dwordx4 v[8:11], v74, s[14:15] offset:2048 nt
	s_mov_b64 exec, s[46:47]
	global_load_dwordx4 v[12:15], v74, s[14:15] offset:3072 nt
	s_add_u32 s14, s14, 0x1000
	s_addc_u32 s15, s15, 0
	s_mov_b64 exec, s[48:49]
	global_load_dwordx4 v[16:19], v74, s[14:15] nt
	s_mov_b64 exec, s[50:51]
	global_load_dwordx4 v[20:23], v74, s[14:15] offset:1024 nt
	s_mov_b64 exec, s[52:53]
	global_load_dwordx4 v[24:27], v74, s[14:15] offset:2048 nt
	s_mov_b64 exec, s[54:55]
	global_load_dwordx4 v[28:31], v74, s[14:15] offset:3072 nt
	s_add_u32 s14, s14, 0x1000
	s_addc_u32 s15, s15, 0
	s_mov_b64 exec, s[56:57]
	global_load_dwordx4 v[32:35], v74, s[14:15] nt
	s_mov_b64 exec, s[58:59]
	global_load_dwordx4 v[36:39], v74, s[14:15] offset:1024 nt
	s_mov_b64 exec, s[60:61]
	global_load_dwordx4 v[40:43], v74, s[14:15] offset:2048 nt
	s_mov_b64 exec, s[62:63]
	global_load_dwordx4 v[44:47], v74, s[14:15] offset:3072 nt
	s_add_u32 s14, s14, 0x1000
	s_addc_u32 s15, s15, 0
	s_mov_b64 exec, s[64:65]
	global_load_dwordx4 v[48:51], v74, s[14:15] nt
	s_mov_b64 exec, s[66:67]
	global_load_dwordx4 v[52:55], v74, s[14:15] offset:1024 nt
	s_mov_b64 exec, s[68:69]
	global_load_dwordx4 v[56:59], v74, s[14:15] offset:2048 nt
	s_mov_b64 exec, s[70:71]
	global_load_dwordx4 v[60:63], v74, s[14:15] offset:3072 nt
	s_mov_b64 exec, -1
	v_mov_b32_e32 v96, 0
	v_mov_b32_e32 v97, 0
	v_mov_b32_e32 v98, 0
	v_mov_b32_e32 v99, 0
	v_mov_b32_e32 v100, 0
	v_mov_b32_e32 v101, 0
	v_mov_b32_e32 v102, 0
	v_mov_b32_e32 v103, 0
	s_waitcnt vmcnt(0)
	s_mov_b64 exec, s[40:41]
	v_pk_fma_f32 v[96:97], v[80:81], v[0:1], v[96:97] op_sel_hi:[0,1,1]
	v_pk_fma_f32 v[98:99], v[80:81], v[2:3], v[98:99] op_sel_hi:[0,1,1]
	s_mov_b64 exec, s[42:43]
	v_pk_fma_f32 v[100:101], v[80:81], v[4:5], v[100:101] op_sel:[1,0,0]
	v_pk_fma_f32 v[102:103], v[80:81], v[6:7], v[102:103] op_sel:[1,0,0]
	s_mov_b64 exec, s[44:45]
	v_pk_fma_f32 v[96:97], v[82:83], v[8:9], v[96:97] op_sel_hi:[0,1,1]
	v_pk_fma_f32 v[98:99], v[82:83], v[10:11], v[98:99] op_sel_hi:[0,1,1]
	s_mov_b64 exec, s[46:47]
	v_pk_fma_f32 v[100:101], v[82:83], v[12:13], v[100:101] op_sel:[1,0,0]
	v_pk_fma_f32 v[102:103], v[82:83], v[14:15], v[102:103] op_sel:[1,0,0]
	s_mov_b64 exec, s[48:49]
	v_pk_fma_f32 v[96:97], v[84:85], v[16:17], v[96:97] op_sel_hi:[0,1,1]
	v_pk_fma_f32 v[98:99], v[84:85], v[18:19], v[98:99] op_sel_hi:[0,1,1]
	s_mov_b64 exec, s[50:51]
	v_pk_fma_f32 v[100:101], v[84:85], v[20:21], v[100:101] op_sel:[1,0,0]
	v_pk_fma_f32 v[102:103], v[84:85], v[22:23], v[102:103] op_sel:[1,0,0]
	s_mov_b64 exec, s[52:53]
	v_pk_fma_f32 v[96:97], v[86:87], v[24:25], v[96:97] op_sel_hi:[0,1,1]
	v_pk_fma_f32 v[98:99], v[86:87], v[26:27], v[98:99] op_sel_hi:[0,1,1]
	s_mov_b64 exec, s[54:55]
	v_pk_fma_f32 v[100:101], v[86:87], v[28:29], v[100:101] op_sel:[1,0,0]
	v_pk_fma_f32 v[102:103], v[86:87], v[30:31], v[102:103] op_sel:[1,0,0]
	s_mov_b64 exec, s[56:57]
	v_pk_fma_f32 v[96:97], v[88:89], v[32:33], v[96:97] op_sel_hi:[0,1,1]
	v_pk_fma_f32 v[98:99], v[88:89], v[34:35], v[98:99] op_sel_hi:[0,1,1]
	s_mov_b64 exec, s[58:59]
	v_pk_fma_f32 v[100:101], v[88:89], v[36:37], v[100:101] op_sel:[1,0,0]
	v_pk_fma_f32 v[102:103], v[88:89], v[38:39], v[102:103] op_sel:[1,0,0]
	s_mov_b64 exec, s[60:61]
	v_pk_fma_f32 v[96:97], v[90:91], v[40:41], v[96:97] op_sel_hi:[0,1,1]
	v_pk_fma_f32 v[98:99], v[90:91], v[42:43], v[98:99] op_sel_hi:[0,1,1]
	s_mov_b64 exec, s[62:63]
	v_pk_fma_f32 v[100:101], v[90:91], v[44:45], v[100:101] op_sel:[1,0,0]
	v_pk_fma_f32 v[102:103], v[90:91], v[46:47], v[102:103] op_sel:[1,0,0]
	s_mov_b64 exec, s[64:65]
	v_pk_fma_f32 v[96:97], v[92:93], v[48:49], v[96:97] op_sel_hi:[0,1,1]
	v_pk_fma_f32 v[98:99], v[92:93], v[50:51], v[98:99] op_sel_hi:[0,1,1]
	s_mov_b64 exec, s[66:67]
	v_pk_fma_f32 v[100:101], v[92:93], v[52:53], v[100:101] op_sel:[1,0,0]
	v_pk_fma_f32 v[102:103], v[92:93], v[54:55], v[102:103] op_sel:[1,0,0]
	s_mov_b64 exec, s[68:69]
	v_pk_fma_f32 v[96:97], v[94:95], v[56:57], v[96:97] op_sel_hi:[0,1,1]
	v_pk_fma_f32 v[98:99], v[94:95], v[58:59], v[98:99] op_sel_hi:[0,1,1]
	s_mov_b64 exec, s[70:71]
	v_pk_fma_f32 v[100:101], v[94:95], v[60:61], v[100:101] op_sel:[1,0,0]
	v_pk_fma_f32 v[102:103], v[94:95], v[62:63], v[102:103] op_sel:[1,0,0]
	s_mov_b64 exec, -1
	ds_read_b128 v[0:3], v74
	ds_read_b128 v[4:7], v74 offset:1024
	ds_read_b128 v[8:11], v74 offset:2048
	ds_read_b128 v[12:15], v74 offset:3072
	ds_read_b128 v[16:19], v74 offset:4096
	ds_read_b128 v[20:23], v74 offset:5120
	ds_read_b128 v[24:27], v74 offset:6144
	ds_read_b128 v[28:31], v74 offset:7168
	ds_read_b128 v[32:35], v74 offset:8192
	ds_read_b128 v[36:39], v74 offset:9216
	ds_read_b128 v[40:43], v74 offset:10240
	ds_read_b128 v[44:47], v74 offset:11264
	ds_read_b128 v[48:51], v74 offset:12288
	ds_read_b128 v[52:55], v74 offset:13312
	ds_read_b128 v[56:59], v74 offset:14336
	v_pk_add_f32 v[96:97], v[96:97], v[100:101]
	v_pk_add_f32 v[98:99], v[98:99], v[102:103]
	s_nop 1
	v_permlane16_swap_b32_e32 v96, v97
	v_permlane16_swap_b32_e32 v98, v99
	v_add_f32_e32 v96, v96, v97
	v_add_f32_e32 v98, v98, v99
	s_nop 1
	v_permlane32_swap_b32_e32 v96, v98
	v_add_f32_e32 v96, v96, v98
	v_add_f32_e32 v96, v96, v73
	s_waitcnt lgkmcnt(5)
	ds_read_b128 v[60:63], v74 offset:15360
	ds_write_b32 v78, v96
	ds_read2_b32 v[80:81], v79 offset0:0 offset1:4
	ds_read2_b32 v[82:83], v79 offset0:8 offset1:12
	ds_read2_b32 v[84:85], v79 offset0:16 offset1:20
	ds_read2_b32 v[86:87], v79 offset0:24 offset1:28
	ds_read2_b32 v[88:89], v79 offset0:32 offset1:36
	ds_read2_b32 v[90:91], v79 offset0:40 offset1:44
	ds_read2_b32 v[92:93], v79 offset0:48 offset1:52
	ds_read2_b32 v[94:95], v79 offset0:56 offset1:60
	v_lshlrev_b32_e32 v72, 3, v76
	v_lshl_or_b32 v72, v75, 2, v72
	v_cmp_gt_u32_e32 vcc, 2, v75
	s_waitcnt lgkmcnt(0)
	v_pk_mul_f32 v[96:97], v[80:81], v[0:1] op_sel_hi:[0,1]
	v_pk_mul_f32 v[98:99], v[80:81], v[2:3] op_sel_hi:[0,1]
	v_pk_mul_f32 v[100:101], v[80:81], v[4:5] op_sel:[1,0]
	v_pk_mul_f32 v[102:103], v[80:81], v[6:7] op_sel:[1,0]
	v_pk_fma_f32 v[96:97], v[82:83], v[8:9], v[96:97] op_sel_hi:[0,1,1]
	v_pk_fma_f32 v[98:99], v[82:83], v[10:11], v[98:99] op_sel_hi:[0,1,1]
	v_pk_fma_f32 v[100:101], v[82:83], v[12:13], v[100:101] op_sel:[1,0,0]
	v_pk_fma_f32 v[102:103], v[82:83], v[14:15], v[102:103] op_sel:[1,0,0]
	v_pk_fma_f32 v[96:97], v[84:85], v[16:17], v[96:97] op_sel_hi:[0,1,1]
	v_pk_fma_f32 v[98:99], v[84:85], v[18:19], v[98:99] op_sel_hi:[0,1,1]
	v_pk_fma_f32 v[100:101], v[84:85], v[20:21], v[100:101] op_sel:[1,0,0]
	v_pk_fma_f32 v[102:103], v[84:85], v[22:23], v[102:103] op_sel:[1,0,0]
	v_pk_fma_f32 v[96:97], v[86:87], v[24:25], v[96:97] op_sel_hi:[0,1,1]
	v_pk_fma_f32 v[98:99], v[86:87], v[26:27], v[98:99] op_sel_hi:[0,1,1]
	v_pk_fma_f32 v[100:101], v[86:87], v[28:29], v[100:101] op_sel:[1,0,0]
	v_pk_fma_f32 v[102:103], v[86:87], v[30:31], v[102:103] op_sel:[1,0,0]
	v_pk_fma_f32 v[96:97], v[88:89], v[32:33], v[96:97] op_sel_hi:[0,1,1]
	v_pk_fma_f32 v[98:99], v[88:89], v[34:35], v[98:99] op_sel_hi:[0,1,1]
	v_pk_fma_f32 v[100:101], v[88:89], v[36:37], v[100:101] op_sel:[1,0,0]
	v_pk_fma_f32 v[102:103], v[88:89], v[38:39], v[102:103] op_sel:[1,0,0]
	v_pk_fma_f32 v[96:97], v[90:91], v[40:41], v[96:97] op_sel_hi:[0,1,1]
	v_pk_fma_f32 v[98:99], v[90:91], v[42:43], v[98:99] op_sel_hi:[0,1,1]
	v_pk_fma_f32 v[100:101], v[90:91], v[44:45], v[100:101] op_sel:[1,0,0]
	v_pk_fma_f32 v[102:103], v[90:91], v[46:47], v[102:103] op_sel:[1,0,0]
	v_pk_fma_f32 v[96:97], v[92:93], v[48:49], v[96:97] op_sel_hi:[0,1,1]
	v_pk_fma_f32 v[98:99], v[92:93], v[50:51], v[98:99] op_sel_hi:[0,1,1]
	v_pk_fma_f32 v[100:101], v[92:93], v[52:53], v[100:101] op_sel:[1,0,0]
	v_pk_fma_f32 v[102:103], v[92:93], v[54:55], v[102:103] op_sel:[1,0,0]
	v_pk_fma_f32 v[96:97], v[94:95], v[56:57], v[96:97] op_sel_hi:[0,1,1]
	v_pk_fma_f32 v[98:99], v[94:95], v[58:59], v[98:99] op_sel_hi:[0,1,1]
	v_pk_fma_f32 v[100:101], v[94:95], v[60:61], v[100:101] op_sel:[1,0,0]
	v_pk_fma_f32 v[102:103], v[94:95], v[62:63], v[102:103] op_sel:[1,0,0]
	v_pk_add_f32 v[96:97], v[96:97], v[100:101]
	v_pk_add_f32 v[98:99], v[98:99], v[102:103]
	s_nop 1
	v_permlane16_swap_b32_e32 v96, v98
	v_permlane16_swap_b32_e32 v97, v99
	v_add_f32_e32 v96, v96, v98
	v_add_f32_e32 v97, v97, v99
	v_mov_b32_e32 v80, v96
	v_mov_b32_e32 v81, v97
	s_nop 1
	v_permlane32_swap_b32_e32 v96, v80
	v_permlane32_swap_b32_e32 v97, v81
	v_add_f32_e32 v96, v96, v80
	v_add_f32_e32 v97, v97, v81
	v_cvt_pk_f16_f32 v73, v96, v97
	s_and_saveexec_b64 s[4:5], vcc
	global_atomic_pk_add_f16 v72, v73, s[20:21]
	s_endpgm
	.p2align	8

	.amdhsa_kernel _Z11edge_kernelILi64ELb0EEvPKfS1_PKDF16_PKiS5_S1_S1_S1_S1_S1_PDF16_
		.amdhsa_group_segment_fixed_size 16896
		.amdhsa_private_segment_fixed_size 0
		.amdhsa_kernarg_size 88
		.amdhsa_user_sgpr_count 2
		.amdhsa_user_sgpr_dispatch_ptr 0
		.amdhsa_user_sgpr_queue_ptr 0
		.amdhsa_user_sgpr_kernarg_segment_ptr 1
		.amdhsa_user_sgpr_dispatch_id 0
		.amdhsa_user_sgpr_kernarg_preload_length 0
		.amdhsa_user_sgpr_kernarg_preload_offset 0
		.amdhsa_user_sgpr_private_segment_size 0
		.amdhsa_uses_dynamic_stack 0
		.amdhsa_enable_private_segment 0
		.amdhsa_system_sgpr_workgroup_id_x 1
		.amdhsa_system_sgpr_workgroup_id_y 0
		.amdhsa_system_sgpr_workgroup_id_z 0
		.amdhsa_system_sgpr_workgroup_info 0
		.amdhsa_system_vgpr_workitem_id 0
		.amdhsa_next_free_vgpr 104
		.amdhsa_next_free_sgpr 96
		.amdhsa_accum_offset 104
		.amdhsa_reserve_vcc 1
		.amdhsa_float_round_mode_32 0
		.amdhsa_float_round_mode_16_64 0
		.amdhsa_float_denorm_mode_32 3
		.amdhsa_float_denorm_mode_16_64 3
		.amdhsa_dx10_clamp 1
		.amdhsa_ieee_mode 1
		.amdhsa_fp16_overflow 0
		.amdhsa_tg_split 0
		.amdhsa_exception_fp_ieee_invalid_op 0
		.amdhsa_exception_fp_denorm_src 0
		.amdhsa_exception_fp_ieee_div_zero 0
		.amdhsa_exception_fp_ieee_overflow 0
		.amdhsa_exception_fp_ieee_underflow 0
		.amdhsa_exception_fp_ieee_inexact 0
		.amdhsa_exception_int_div_zero 0
	.end_amdhsa_kernel

amdhsa.kernels:
  - .agpr_count:     8
    .args:
      - .actual_access:  read_only
        .address_space:  global
        .offset:         0
        .size:           8
        .value_kind:     global_buffer
      - .actual_access:  read_only
        .address_space:  global
        .offset:         8
        .size:           8
        .value_kind:     global_buffer
      - .actual_access:  read_only
        .address_space:  global
        .offset:         16
        .size:           8
        .value_kind:     global_buffer
      - .actual_access:  read_only
        .address_space:  global
        .offset:         24
        .size:           8
        .value_kind:     global_buffer
      - .actual_access:  write_only
        .address_space:  global
        .offset:         32
        .size:           8
        .value_kind:     global_buffer
      - .actual_access:  write_only
        .address_space:  global
        .offset:         40
        .size:           8
        .value_kind:     global_buffer
    .group_segment_fixed_size: 4224
    .kernarg_segment_align: 8
    .kernarg_segment_size: 48
    .language:       OpenCL C
    .language_version:
      - 2
      - 0
    .max_flat_workgroup_size: 128
    .name:           _Z11init_kernelPKfS0_S0_S0_PDF16_S1_
    .private_segment_fixed_size: 0
    .sgpr_count:     30
    .sgpr_spill_count: 0
    .symbol:         _Z11init_kernelPKfS0_S0_S0_PDF16_S1_.kd
    .uniform_work_group_size: 1
    .uses_dynamic_stack: false
    .vgpr_count:     68
    .vgpr_spill_count: 0
    .wavefront_size: 64
  - .agpr_count:     8
    .args:
      - .actual_access:  read_only
        .address_space:  global
        .offset:         0
        .size:           8
        .value_kind:     global_buffer
      - .actual_access:  read_only
        .address_space:  global
        .offset:         8
        .size:           8
        .value_kind:     global_buffer
      - .actual_access:  read_only
        .address_space:  global
        .offset:         16
        .size:           8
        .value_kind:     global_buffer
      - .actual_access:  read_only
        .address_space:  global
        .offset:         24
        .size:           8
        .value_kind:     global_buffer
      - .actual_access:  read_only
        .address_space:  global
        .offset:         32
        .size:           8
        .value_kind:     global_buffer
      - .actual_access:  read_only
        .address_space:  global
        .offset:         40
        .size:           8
        .value_kind:     global_buffer
      - .actual_access:  write_only
        .address_space:  global
        .offset:         48
        .size:           8
        .value_kind:     global_buffer
    .group_segment_fixed_size: 4352
    .kernarg_segment_align: 8
    .kernarg_segment_size: 56
    .language:       OpenCL C
    .language_version:
      - 2
      - 0
    .max_flat_workgroup_size: 128
    .name:           _Z12final_kernelPKDF16_S0_PKfS2_S2_S2_Pf
    .private_segment_fixed_size: 0
    .sgpr_count:     30
    .sgpr_spill_count: 0
    .symbol:         _Z12final_kernelPKDF16_S0_PKfS2_S2_S2_Pf.kd
    .uniform_work_group_size: 1
    .uses_dynamic_stack: false
    .vgpr_count:     88
    .vgpr_spill_count: 0
    .wavefront_size: 64
  - .agpr_count:     0
    .args:
      - .actual_access:  read_only
        .address_space:  global
        .offset:         0
        .size:           8
        .value_kind:     global_buffer
      - .actual_access:  read_only
        .address_space:  global
        .offset:         8
        .size:           8
        .value_kind:     global_buffer
      - .actual_access:  read_only
        .address_space:  global
        .offset:         16
        .size:           8
        .value_kind:     global_buffer
      - .actual_access:  read_only
        .address_space:  global
        .offset:         24
        .size:           8
        .value_kind:     global_buffer
      - .actual_access:  read_only
        .address_space:  global
        .offset:         32
        .size:           8
        .value_kind:     global_buffer
      - .actual_access:  read_only
        .address_space:  global
        .offset:         40
        .size:           8
        .value_kind:     global_buffer
      - .actual_access:  read_only
        .address_space:  global
        .offset:         48
        .size:           8
        .value_kind:     global_buffer
      - .actual_access:  read_only
        .address_space:  global
        .offset:         56
        .size:           8
        .value_kind:     global_buffer
      - .actual_access:  read_only
        .address_space:  global
        .offset:         64
        .size:           8
        .value_kind:     global_buffer
      - .actual_access:  read_only
        .address_space:  global
        .offset:         72
        .size:           8
        .value_kind:     global_buffer
      - .address_space:  global
        .offset:         80
        .size:           8
        .value_kind:     global_buffer
    .group_segment_fixed_size: 16896
    .kernarg_segment_align: 8
    .kernarg_segment_size: 88
    .language:       OpenCL C
    .language_version:
      - 2
      - 0
    .max_flat_workgroup_size: 128
    .name:           _Z11edge_kernelILi36ELb1EEvPKfS1_PKDF16_PKiS5_S1_S1_S1_S1_S1_PDF16_
    .private_segment_fixed_size: 0
    .sgpr_count:     45
    .sgpr_spill_count: 0
    .symbol:         _Z11edge_kernelILi36ELb1EEvPKfS1_PKDF16_PKiS5_S1_S1_S1_S1_S1_PDF16_.kd
    .uniform_work_group_size: 1
    .uses_dynamic_stack: false
    .vgpr_count:     104
    .vgpr_spill_count: 0
    .wavefront_size: 64
  - .agpr_count:     0
    .args:
      - .actual_access:  read_only
        .address_space:  global
        .offset:         0
        .size:           8
        .value_kind:     global_buffer
      - .actual_access:  read_only
        .address_space:  global
        .offset:         8
        .size:           8
        .value_kind:     global_buffer
      - .actual_access:  read_only
        .address_space:  global
        .offset:         16
        .size:           8
        .value_kind:     global_buffer
      - .actual_access:  read_only
        .address_space:  global
        .offset:         24
        .size:           8
        .value_kind:     global_buffer
      - .actual_access:  read_only
        .address_space:  global
        .offset:         32
        .size:           8
        .value_kind:     global_buffer
      - .actual_access:  read_only
        .address_space:  global
        .offset:         40
        .size:           8
        .value_kind:     global_buffer
      - .actual_access:  read_only
        .address_space:  global
        .offset:         48
        .size:           8
        .value_kind:     global_buffer
      - .actual_access:  read_only
        .address_space:  global
        .offset:         56
        .size:           8
        .value_kind:     global_buffer
      - .actual_access:  read_only
        .address_space:  global
        .offset:         64
        .size:           8
        .value_kind:     global_buffer
      - .actual_access:  read_only
        .address_space:  global
        .offset:         72
        .size:           8
        .value_kind:     global_buffer
      - .address_space:  global
        .offset:         80
        .size:           8
        .value_kind:     global_buffer
    .group_segment_fixed_size: 16896
    .kernarg_segment_align: 8
    .kernarg_segment_size: 88
    .language:       OpenCL C
    .language_version:
      - 2
      - 0
    .max_flat_workgroup_size: 128
    .name:           _Z11edge_kernelILi64ELb0EEvPKfS1_PKDF16_PKiS5_S1_S1_S1_S1_S1_PDF16_
    .private_segment_fixed_size: 0
    .sgpr_count:     44
    .sgpr_spill_count: 0
    .symbol:         _Z11edge_kernelILi64ELb0EEvPKfS1_PKDF16_PKiS5_S1_S1_S1_S1_S1_PDF16_.kd
    .uniform_work_group_size: 1
    .uses_dynamic_stack: false
    .vgpr_count:     104
    .vgpr_spill_count: 0
    .wavefront_size: 64
